# v19 + MoE up/down: wr1 restore barrier moved after the next-unit lookup (S.next chain and tok gather overlap the wait)
# baseline (speedup 1.0000x reference)
.LBB0_1338:
	s_cmp_lt_u32 s43, 2
	s_cbranch_scc1 .Lup_norestore
	s_andn2_b64 vcc, exec, s[48:49]
	s_cbranch_vccnz .Lup_norestore
	s_barrier

.LBB0_1342:
	s_waitcnt vmcnt(0)
	v_mov_b32_e32 v154, v79
	v_mov_b32_e32 v155, v81
	v_pk_add_f32 v[160:161], v[154:155], 1.0 op_sel_hi:[1,0]
	v_mov_b32_e32 v154, v75
	v_mov_b32_e32 v155, v77
	v_pk_add_f32 v[158:159], v[154:155], 1.0 op_sel_hi:[1,0]
	v_mov_b32_e32 v154, v63
	v_mov_b32_e32 v63, v64
	v_mov_b32_e32 v155, v65
	v_mov_b32_e32 v79, v80
	v_pk_add_f32 v[64:65], v[134:135], v[62:63]
	v_pk_add_f32 v[80:81], v[142:143], v[78:79]
	s_mov_b32 s34, 0xc01d265f
	v_min_f32_e32 v65, 0x40e00000, v65
	v_min_f32_e32 v64, 0x40e00000, v64
	v_min_f32_e32 v81, 0x40e00000, v81
	v_min_f32_e32 v80, 0x40e00000, v80
	v_pk_mul_f32 v[134:135], v[64:65], s[34:35] op_sel_hi:[1,0]
	v_pk_mul_f32 v[142:143], v[80:81], s[34:35] op_sel_hi:[1,0]
	v_exp_f32_e32 v134, v134
	v_exp_f32_e32 v135, v135
	v_exp_f32_e32 v142, v142
	v_exp_f32_e32 v143, v143
	v_pk_add_f32 v[156:157], v[154:155], 1.0 op_sel_hi:[1,0]
	v_pk_add_f32 v[134:135], v[134:135], 1.0 op_sel_hi:[1,0]
	v_mov_b32_e32 v154, v59
	v_pk_add_f32 v[142:143], v[142:143], 1.0 op_sel_hi:[1,0]
	v_rcp_f32_e32 v134, v134
	v_rcp_f32_e32 v135, v135
	v_rcp_f32_e32 v142, v142
	v_rcp_f32_e32 v143, v143
	v_mov_b32_e32 v59, v60
	v_mov_b32_e32 v155, v61
	v_mov_b32_e32 v75, v76
	v_pk_add_f32 v[130:131], v[130:131], v[156:157]
	v_pk_add_f32 v[60:61], v[136:137], v[58:59]
	v_pk_add_f32 v[154:155], v[154:155], 1.0 op_sel_hi:[1,0]
	v_pk_add_f32 v[138:139], v[138:139], v[160:161]
	v_pk_add_f32 v[76:77], v[144:145], v[74:75]
	v_med3_f32 v130, v130, s89, v238
	v_med3_f32 v131, v131, s89, v238
	v_pk_mul_f32 v[64:65], v[64:65], v[134:135]
	v_min_f32_e32 v61, 0x40e00000, v61
	v_min_f32_e32 v60, 0x40e00000, v60
	v_med3_f32 v138, v138, s89, v238
	v_med3_f32 v139, v139, s89, v238
	v_pk_mul_f32 v[80:81], v[80:81], v[142:143]
	v_min_f32_e32 v77, 0x40e00000, v77
	v_min_f32_e32 v76, 0x40e00000, v76
	v_pk_mul_f32 v[64:65], v[130:131], v[64:65]
	v_pk_add_f32 v[130:131], v[132:133], v[154:155]
	v_pk_mul_f32 v[132:133], v[60:61], s[34:35] op_sel_hi:[1,0]
	v_pk_mul_f32 v[80:81], v[138:139], v[80:81]
	v_pk_add_f32 v[138:139], v[140:141], v[158:159]
	v_pk_mul_f32 v[140:141], v[76:77], s[34:35] op_sel_hi:[1,0]
	v_exp_f32_e32 v132, v132
	v_exp_f32_e32 v133, v133
	v_exp_f32_e32 v140, v140
	v_exp_f32_e32 v141, v141
	s_lshl_b32 s1, s60, 7
	s_or_b32 s40, s1, s77
	s_lshl_b32 s1, s45, 8
	v_pk_add_f32 v[132:133], v[132:133], 1.0 op_sel_hi:[1,0]
	s_add_i32 s60, s1, s76
	v_pk_add_f32 v[140:141], v[140:141], 1.0 op_sel_hi:[1,0]
	v_rcp_f32_e32 v132, v132
	v_rcp_f32_e32 v133, v133
	s_ashr_i32 s61, s60, 31
	s_ashr_i32 s41, s40, 31
	v_rcp_f32_e32 v140, v140
	v_rcp_f32_e32 v141, v141
	s_lshl_b64 s[14:15], s[60:61], 11
	s_add_u32 s2, s78, s14
	s_addc_u32 s15, s79, s15
	s_lshl_b64 s[40:41], s[40:41], 1
	v_med3_f32 v130, v130, s89, v238
	v_med3_f32 v131, v131, s89, v238
	v_pk_mul_f32 v[60:61], v[60:61], v[132:133]
	s_add_u32 s14, s2, s40
	v_med3_f32 v138, v138, s89, v238
	v_med3_f32 v139, v139, s89, v238
	v_pk_mul_f32 v[76:77], v[76:77], v[140:141]
	v_pk_mul_f32 v[60:61], v[130:131], v[60:61]
	s_addc_u32 s15, s15, s41
	v_pk_mul_f32 v[76:77], v[138:139], v[76:77]
	v_cvt_pk_bf16_f32 v130, v80, v81
	v_pk_add_f32 v[54:55], v[54:55], v[62:63]
	v_cvt_pk_bf16_f32 v131, v76, v77
	v_cvt_pk_bf16_f32 v132, v64, v65
	v_cvt_pk_bf16_f32 v133, v60, v61
	v_lshl_add_u64 v[60:61], s[14:15], 0, v[152:153]
	global_store_dwordx4 v[60:61], v[130:133], off
	v_pk_add_f32 v[60:61], v[126:127], v[78:79]
	v_pk_add_f32 v[64:65], v[122:123], v[160:161]
	v_min_f32_e32 v61, 0x40e00000, v61
	v_min_f32_e32 v60, 0x40e00000, v60
	v_pk_mul_f32 v[76:77], v[60:61], s[34:35] op_sel_hi:[1,0]
	v_med3_f32 v64, v64, s89, v238
	v_exp_f32_e32 v76, v76
	v_exp_f32_e32 v77, v77
	v_med3_f32 v65, v65, s89, v238
	s_add_i32 s14, s85, s1
	s_ashr_i32 s15, s14, 31
	v_pk_add_f32 v[76:77], v[76:77], 1.0 op_sel_hi:[1,0]
	s_lshl_b64 s[14:15], s[14:15], 11
	v_rcp_f32_e32 v76, v76
	v_rcp_f32_e32 v77, v77
	s_add_u32 s2, s78, s14
	s_addc_u32 s15, s79, s15
	s_add_u32 s14, s2, s40
	v_pk_mul_f32 v[60:61], v[60:61], v[76:77]
	v_pk_add_f32 v[76:77], v[124:125], v[158:159]
	v_pk_mul_f32 v[60:61], v[64:65], v[60:61]
	v_pk_add_f32 v[64:65], v[128:129], v[74:75]
	v_med3_f32 v76, v76, s89, v238
	v_min_f32_e32 v65, 0x40e00000, v65
	v_min_f32_e32 v64, 0x40e00000, v64
	v_pk_mul_f32 v[80:81], v[64:65], s[34:35] op_sel_hi:[1,0]
	v_med3_f32 v77, v77, s89, v238
	v_exp_f32_e32 v80, v80
	v_exp_f32_e32 v81, v81
	s_addc_u32 s15, s15, s41
	v_min_f32_e32 v55, 0x40e00000, v55
	v_min_f32_e32 v54, 0x40e00000, v54
	v_pk_add_f32 v[80:81], v[80:81], 1.0 op_sel_hi:[1,0]
	v_pk_add_f32 v[50:51], v[50:51], v[156:157]
	v_rcp_f32_e32 v80, v80
	v_rcp_f32_e32 v81, v81
	v_med3_f32 v50, v50, s89, v238
	v_med3_f32 v51, v51, s89, v238
	v_pk_add_f32 v[52:53], v[52:53], v[154:155]
	v_pk_mul_f32 v[64:65], v[64:65], v[80:81]
	v_pk_add_f32 v[80:81], v[114:115], v[156:157]
	v_pk_mul_f32 v[64:65], v[76:77], v[64:65]
	v_pk_add_f32 v[76:77], v[118:119], v[62:63]
	v_med3_f32 v80, v80, s89, v238
	v_min_f32_e32 v77, 0x40e00000, v77
	v_min_f32_e32 v76, 0x40e00000, v76
	v_pk_mul_f32 v[114:115], v[76:77], s[34:35] op_sel_hi:[1,0]
	v_med3_f32 v81, v81, s89, v238
	v_exp_f32_e32 v114, v114
	v_exp_f32_e32 v115, v115
	v_med3_f32 v52, v52, s89, v238
	v_med3_f32 v53, v53, s89, v238
	v_pk_add_f32 v[46:47], v[46:47], v[78:79]
	v_pk_add_f32 v[114:115], v[114:115], 1.0 op_sel_hi:[1,0]
	v_min_f32_e32 v47, 0x40e00000, v47
	v_rcp_f32_e32 v114, v114
	v_rcp_f32_e32 v115, v115
	v_min_f32_e32 v46, 0x40e00000, v46
	v_pk_add_f32 v[42:43], v[42:43], v[160:161]
	v_pk_add_f32 v[44:45], v[44:45], v[158:159]
	v_pk_mul_f32 v[76:77], v[76:77], v[114:115]
	v_pk_add_f32 v[114:115], v[116:117], v[154:155]
	v_pk_mul_f32 v[76:77], v[80:81], v[76:77]
	v_pk_add_f32 v[80:81], v[120:121], v[58:59]
	v_med3_f32 v114, v114, s89, v238
	v_min_f32_e32 v81, 0x40e00000, v81
	v_min_f32_e32 v80, 0x40e00000, v80
	v_pk_mul_f32 v[116:117], v[80:81], s[34:35] op_sel_hi:[1,0]
	v_med3_f32 v115, v115, s89, v238
	v_exp_f32_e32 v116, v116
	v_exp_f32_e32 v117, v117
	v_med3_f32 v42, v42, s89, v238
	v_med3_f32 v43, v43, s89, v238
	v_pk_add_f32 v[38:39], v[38:39], v[62:63]
	v_pk_add_f32 v[116:117], v[116:117], 1.0 op_sel_hi:[1,0]
	v_med3_f32 v44, v44, s89, v238
	v_rcp_f32_e32 v116, v116
	v_rcp_f32_e32 v117, v117
	v_med3_f32 v45, v45, s89, v238
	v_min_f32_e32 v39, 0x40e00000, v39
	v_min_f32_e32 v38, 0x40e00000, v38
	v_pk_mul_f32 v[80:81], v[80:81], v[116:117]
	v_pk_add_f32 v[34:35], v[34:35], v[156:157]
	v_pk_mul_f32 v[80:81], v[114:115], v[80:81]
	v_cvt_pk_bf16_f32 v114, v60, v61
	v_lshl_add_u64 v[60:61], s[14:15], 0, v[152:153]
	v_cvt_pk_bf16_f32 v115, v64, v65
	v_cvt_pk_bf16_f32 v116, v76, v77
	v_cvt_pk_bf16_f32 v117, v80, v81
	global_store_dwordx4 v[60:61], v[114:117], off
	v_pk_add_f32 v[60:61], v[110:111], v[78:79]
	v_pk_add_f32 v[64:65], v[106:107], v[160:161]
	v_min_f32_e32 v61, 0x40e00000, v61
	v_min_f32_e32 v60, 0x40e00000, v60
	v_pk_mul_f32 v[76:77], v[60:61], s[34:35] op_sel_hi:[1,0]
	v_med3_f32 v64, v64, s89, v238
	v_exp_f32_e32 v76, v76
	v_exp_f32_e32 v77, v77
	v_med3_f32 v65, v65, s89, v238
	s_add_i32 s14, s90, s1
	s_ashr_i32 s15, s14, 31
	v_pk_add_f32 v[76:77], v[76:77], 1.0 op_sel_hi:[1,0]
	s_lshl_b64 s[14:15], s[14:15], 11
	v_rcp_f32_e32 v76, v76
	v_rcp_f32_e32 v77, v77
	s_add_u32 s2, s78, s14
	s_addc_u32 s15, s79, s15
	s_add_u32 s14, s2, s40
	v_pk_mul_f32 v[60:61], v[60:61], v[76:77]
	v_pk_add_f32 v[76:77], v[108:109], v[158:159]
	v_pk_mul_f32 v[60:61], v[64:65], v[60:61]
	v_pk_add_f32 v[64:65], v[112:113], v[74:75]
	v_med3_f32 v76, v76, s89, v238
	v_min_f32_e32 v65, 0x40e00000, v65
	v_min_f32_e32 v64, 0x40e00000, v64
	v_pk_mul_f32 v[80:81], v[64:65], s[34:35] op_sel_hi:[1,0]
	v_med3_f32 v77, v77, s89, v238
	v_exp_f32_e32 v80, v80
	v_exp_f32_e32 v81, v81
	s_addc_u32 s15, s15, s41
	v_med3_f32 v34, v34, s89, v238
	v_med3_f32 v35, v35, s89, v238
	v_pk_add_f32 v[80:81], v[80:81], 1.0 op_sel_hi:[1,0]
	v_pk_add_f32 v[36:37], v[36:37], v[154:155]
	v_rcp_f32_e32 v80, v80
	v_rcp_f32_e32 v81, v81
	v_med3_f32 v36, v36, s89, v238
	v_med3_f32 v37, v37, s89, v238
	v_pk_add_f32 v[30:31], v[30:31], v[78:79]
	v_pk_mul_f32 v[64:65], v[64:65], v[80:81]
	v_pk_add_f32 v[80:81], v[98:99], v[156:157]
	v_pk_mul_f32 v[64:65], v[76:77], v[64:65]
	v_pk_add_f32 v[76:77], v[102:103], v[62:63]
	v_med3_f32 v80, v80, s89, v238
	v_min_f32_e32 v77, 0x40e00000, v77
	v_min_f32_e32 v76, 0x40e00000, v76
	v_pk_mul_f32 v[98:99], v[76:77], s[34:35] op_sel_hi:[1,0]
	v_med3_f32 v81, v81, s89, v238
	v_exp_f32_e32 v98, v98
	v_exp_f32_e32 v99, v99
	v_min_f32_e32 v31, 0x40e00000, v31
	v_min_f32_e32 v30, 0x40e00000, v30
	v_pk_add_f32 v[26:27], v[26:27], v[160:161]
	v_pk_add_f32 v[98:99], v[98:99], 1.0 op_sel_hi:[1,0]
	v_med3_f32 v26, v26, s89, v238
	v_rcp_f32_e32 v98, v98
	v_rcp_f32_e32 v99, v99
	v_med3_f32 v27, v27, s89, v238
	v_pk_add_f32 v[28:29], v[28:29], v[158:159]
	v_pk_add_f32 v[22:23], v[22:23], v[62:63]
	v_pk_mul_f32 v[76:77], v[76:77], v[98:99]
	v_pk_add_f32 v[98:99], v[100:101], v[154:155]
	v_pk_mul_f32 v[76:77], v[80:81], v[76:77]
	v_pk_add_f32 v[80:81], v[104:105], v[58:59]
	v_med3_f32 v98, v98, s89, v238
	v_min_f32_e32 v81, 0x40e00000, v81
	v_min_f32_e32 v80, 0x40e00000, v80
	v_pk_mul_f32 v[100:101], v[80:81], s[34:35] op_sel_hi:[1,0]
	v_med3_f32 v99, v99, s89, v238
	v_exp_f32_e32 v100, v100
	v_exp_f32_e32 v101, v101
	v_med3_f32 v28, v28, s89, v238
	v_med3_f32 v29, v29, s89, v238
	v_min_f32_e32 v23, 0x40e00000, v23
	v_pk_add_f32 v[100:101], v[100:101], 1.0 op_sel_hi:[1,0]
	v_min_f32_e32 v22, 0x40e00000, v22
	v_rcp_f32_e32 v100, v100
	v_rcp_f32_e32 v101, v101
	v_pk_add_f32 v[18:19], v[18:19], v[156:157]
	v_pk_add_f32 v[20:21], v[20:21], v[154:155]
	v_med3_f32 v18, v18, s89, v238
	v_pk_mul_f32 v[80:81], v[80:81], v[100:101]
	v_med3_f32 v19, v19, s89, v238
	v_pk_mul_f32 v[80:81], v[98:99], v[80:81]
	v_cvt_pk_bf16_f32 v98, v60, v61
	v_lshl_add_u64 v[60:61], s[14:15], 0, v[152:153]
	v_cvt_pk_bf16_f32 v99, v64, v65
	v_cvt_pk_bf16_f32 v100, v76, v77
	v_cvt_pk_bf16_f32 v101, v80, v81
	global_store_dwordx4 v[60:61], v[98:101], off
	v_pk_add_f32 v[60:61], v[94:95], v[78:79]
	v_pk_add_f32 v[64:65], v[90:91], v[160:161]
	v_min_f32_e32 v61, 0x40e00000, v61
	v_min_f32_e32 v60, 0x40e00000, v60
	v_pk_mul_f32 v[76:77], v[60:61], s[34:35] op_sel_hi:[1,0]
	v_med3_f32 v64, v64, s89, v238
	v_exp_f32_e32 v76, v76
	v_exp_f32_e32 v77, v77
	v_med3_f32 v65, v65, s89, v238
	s_add_i32 s14, s91, s1
	s_ashr_i32 s15, s14, 31
	v_pk_add_f32 v[76:77], v[76:77], 1.0 op_sel_hi:[1,0]
	s_lshl_b64 s[14:15], s[14:15], 11
	v_rcp_f32_e32 v76, v76
	v_rcp_f32_e32 v77, v77
	s_add_u32 s1, s78, s14
	s_addc_u32 s2, s79, s15
	s_add_u32 s14, s1, s40
	v_pk_mul_f32 v[60:61], v[60:61], v[76:77]
	v_pk_add_f32 v[76:77], v[92:93], v[158:159]
	v_pk_mul_f32 v[60:61], v[64:65], v[60:61]
	v_pk_add_f32 v[64:65], v[96:97], v[74:75]
	v_med3_f32 v76, v76, s89, v238
	v_min_f32_e32 v65, 0x40e00000, v65
	v_min_f32_e32 v64, 0x40e00000, v64
	v_pk_mul_f32 v[80:81], v[64:65], s[34:35] op_sel_hi:[1,0]
	v_med3_f32 v77, v77, s89, v238
	v_exp_f32_e32 v80, v80
	v_exp_f32_e32 v81, v81
	s_addc_u32 s15, s2, s41
	v_med3_f32 v20, v20, s89, v238
	v_med3_f32 v21, v21, s89, v238
	v_pk_add_f32 v[80:81], v[80:81], 1.0 op_sel_hi:[1,0]
	v_pk_add_f32 v[14:15], v[14:15], v[78:79]
	v_rcp_f32_e32 v80, v80
	v_rcp_f32_e32 v81, v81
	v_min_f32_e32 v15, 0x40e00000, v15
	v_min_f32_e32 v14, 0x40e00000, v14
	v_pk_add_f32 v[10:11], v[10:11], v[160:161]
	v_pk_mul_f32 v[64:65], v[64:65], v[80:81]
	v_pk_add_f32 v[80:81], v[82:83], v[156:157]
	v_pk_mul_f32 v[64:65], v[76:77], v[64:65]
	v_pk_add_f32 v[76:77], v[86:87], v[62:63]
	v_med3_f32 v80, v80, s89, v238
	v_min_f32_e32 v77, 0x40e00000, v77
	v_min_f32_e32 v76, 0x40e00000, v76
	v_pk_mul_f32 v[82:83], v[76:77], s[34:35] op_sel_hi:[1,0]
	v_med3_f32 v81, v81, s89, v238
	v_exp_f32_e32 v82, v82
	v_exp_f32_e32 v83, v83
	v_med3_f32 v10, v10, s89, v238
	v_med3_f32 v11, v11, s89, v238
	v_pk_add_f32 v[12:13], v[12:13], v[158:159]
	v_pk_add_f32 v[82:83], v[82:83], 1.0 op_sel_hi:[1,0]
	v_pk_add_f32 v[6:7], v[6:7], v[62:63]
	v_rcp_f32_e32 v82, v82
	v_rcp_f32_e32 v83, v83
	v_med3_f32 v12, v12, s89, v238
	v_med3_f32 v13, v13, s89, v238
	v_min_f32_e32 v7, 0x40e00000, v7
	v_pk_mul_f32 v[76:77], v[76:77], v[82:83]
	v_pk_add_f32 v[82:83], v[84:85], v[154:155]
	v_pk_mul_f32 v[76:77], v[80:81], v[76:77]
	v_pk_add_f32 v[80:81], v[88:89], v[58:59]
	v_med3_f32 v82, v82, s89, v238
	v_min_f32_e32 v81, 0x40e00000, v81
	v_min_f32_e32 v80, 0x40e00000, v80
	v_pk_mul_f32 v[84:85], v[80:81], s[34:35] op_sel_hi:[1,0]
	v_med3_f32 v83, v83, s89, v238
	v_exp_f32_e32 v84, v84
	v_exp_f32_e32 v85, v85
	v_min_f32_e32 v6, 0x40e00000, v6
	v_pk_add_f32 v[2:3], v[2:3], v[156:157]
	v_pk_add_f32 v[4:5], v[4:5], v[154:155]
	v_pk_add_f32 v[84:85], v[84:85], 1.0 op_sel_hi:[1,0]
	v_med3_f32 v2, v2, s89, v238
	v_rcp_f32_e32 v84, v84
	v_rcp_f32_e32 v85, v85
	v_med3_f32 v3, v3, s89, v238
	v_med3_f32 v4, v4, s89, v238
	v_med3_f32 v5, v5, s89, v238
	v_pk_mul_f32 v[80:81], v[80:81], v[84:85]
	s_nop 0
	v_pk_mul_f32 v[84:85], v[82:83], v[80:81]
	v_cvt_pk_bf16_f32 v80, v60, v61
	v_lshl_add_u64 v[60:61], s[14:15], 0, v[152:153]
	v_cvt_pk_bf16_f32 v81, v64, v65
	v_cvt_pk_bf16_f32 v82, v76, v77
	v_cvt_pk_bf16_f32 v83, v84, v85
	global_store_dwordx4 v[60:61], v[80:83], off
	v_pk_add_f32 v[60:61], v[70:71], v[78:79]
	v_pk_add_f32 v[64:65], v[66:67], v[160:161]
	v_min_f32_e32 v61, 0x40e00000, v61
	v_min_f32_e32 v60, 0x40e00000, v60
	v_pk_mul_f32 v[66:67], v[60:61], s[34:35] op_sel_hi:[1,0]
	v_med3_f32 v64, v64, s89, v238
	v_exp_f32_e32 v66, v66
	v_exp_f32_e32 v67, v67
	v_med3_f32 v65, v65, s89, v238
	s_add_i32 s14, s60, 0x80
	s_ashr_i32 s15, s14, 31
	v_pk_add_f32 v[66:67], v[66:67], 1.0 op_sel_hi:[1,0]
	s_lshl_b64 s[14:15], s[14:15], 11
	v_rcp_f32_e32 v66, v66
	v_rcp_f32_e32 v67, v67
	s_add_u32 s1, s78, s14
	s_addc_u32 s2, s79, s15
	s_add_u32 s14, s1, s40
	v_pk_mul_f32 v[60:61], v[60:61], v[66:67]
	v_pk_add_f32 v[66:67], v[68:69], v[158:159]
	v_pk_mul_f32 v[60:61], v[64:65], v[60:61]
	v_pk_add_f32 v[64:65], v[72:73], v[74:75]
	v_med3_f32 v66, v66, s89, v238
	v_min_f32_e32 v65, 0x40e00000, v65
	v_min_f32_e32 v64, 0x40e00000, v64
	v_pk_mul_f32 v[68:69], v[64:65], s[34:35] op_sel_hi:[1,0]
	v_med3_f32 v67, v67, s89, v238
	v_exp_f32_e32 v68, v68
	v_exp_f32_e32 v69, v69
	s_addc_u32 s15, s2, s41
	v_pk_add_f32 v[68:69], v[68:69], 1.0 op_sel_hi:[1,0]
	s_nop 0
	v_rcp_f32_e32 v68, v68
	v_rcp_f32_e32 v69, v69
	s_nop 0
	v_pk_mul_f32 v[64:65], v[64:65], v[68:69]
	s_nop 0
	v_pk_mul_f32 v[64:65], v[66:67], v[64:65]
	v_pk_mul_f32 v[66:67], v[54:55], s[34:35] op_sel_hi:[1,0]
	s_nop 0
	v_exp_f32_e32 v66, v66
	v_exp_f32_e32 v67, v67
	s_nop 0
	v_pk_add_f32 v[66:67], v[66:67], 1.0 op_sel_hi:[1,0]
	s_nop 0
	v_rcp_f32_e32 v66, v66
	v_rcp_f32_e32 v67, v67
	s_nop 0
	v_pk_mul_f32 v[54:55], v[54:55], v[66:67]
	s_nop 0
	v_pk_mul_f32 v[54:55], v[50:51], v[54:55]
	v_pk_add_f32 v[50:51], v[56:57], v[58:59]
	s_nop 0
	v_min_f32_e32 v51, 0x40e00000, v51
	v_min_f32_e32 v50, 0x40e00000, v50
	v_pk_mul_f32 v[56:57], v[50:51], s[34:35] op_sel_hi:[1,0]
	s_nop 0
	v_exp_f32_e32 v56, v56
	v_exp_f32_e32 v57, v57
	s_nop 0
	v_pk_add_f32 v[56:57], v[56:57], 1.0 op_sel_hi:[1,0]
	s_nop 0
	v_rcp_f32_e32 v56, v56
	v_rcp_f32_e32 v57, v57
	s_nop 0
	v_pk_mul_f32 v[50:51], v[50:51], v[56:57]
	s_nop 0
	v_pk_mul_f32 v[56:57], v[52:53], v[50:51]
	v_cvt_pk_bf16_f32 v50, v60, v61
	v_cvt_pk_bf16_f32 v51, v64, v65
	v_cvt_pk_bf16_f32 v52, v54, v55
	v_lshl_add_u64 v[54:55], s[14:15], 0, v[152:153]
	v_cvt_pk_bf16_f32 v53, v56, v57
	global_store_dwordx4 v[54:55], v[50:53], off
	s_add_i32 s14, s60, 0x90
	s_ashr_i32 s15, s14, 31
	v_pk_mul_f32 v[50:51], v[46:47], s[34:35] op_sel_hi:[1,0]
	s_lshl_b64 s[14:15], s[14:15], 11
	v_exp_f32_e32 v50, v50
	v_exp_f32_e32 v51, v51
	s_add_u32 s1, s78, s14
	s_addc_u32 s2, s79, s15
	s_add_u32 s14, s1, s40
	v_pk_add_f32 v[50:51], v[50:51], 1.0 op_sel_hi:[1,0]
	s_addc_u32 s15, s2, s41
	v_rcp_f32_e32 v50, v50
	v_rcp_f32_e32 v51, v51
	s_nop 0
	v_pk_mul_f32 v[46:47], v[46:47], v[50:51]
	s_nop 0
	v_pk_mul_f32 v[42:43], v[42:43], v[46:47]
	v_pk_add_f32 v[46:47], v[48:49], v[74:75]
	s_nop 0
	v_min_f32_e32 v47, 0x40e00000, v47
	v_min_f32_e32 v46, 0x40e00000, v46
	v_pk_mul_f32 v[48:49], v[46:47], s[34:35] op_sel_hi:[1,0]
	s_nop 0
	v_exp_f32_e32 v48, v48
	v_exp_f32_e32 v49, v49
	s_nop 0
	v_pk_add_f32 v[48:49], v[48:49], 1.0 op_sel_hi:[1,0]
	s_nop 0
	v_rcp_f32_e32 v48, v48
	v_rcp_f32_e32 v49, v49
	s_nop 0
	v_pk_mul_f32 v[46:47], v[46:47], v[48:49]
	s_nop 0
	v_pk_mul_f32 v[44:45], v[44:45], v[46:47]
	v_pk_mul_f32 v[46:47], v[38:39], s[34:35] op_sel_hi:[1,0]
	s_nop 0
	v_exp_f32_e32 v46, v46
	v_exp_f32_e32 v47, v47
	s_nop 0
	v_pk_add_f32 v[46:47], v[46:47], 1.0 op_sel_hi:[1,0]
	s_nop 0
	v_rcp_f32_e32 v46, v46
	v_rcp_f32_e32 v47, v47
	s_nop 0
	v_pk_mul_f32 v[38:39], v[38:39], v[46:47]
	s_nop 0
	v_pk_mul_f32 v[38:39], v[34:35], v[38:39]
	v_pk_add_f32 v[34:35], v[40:41], v[58:59]
	s_nop 0
	v_min_f32_e32 v35, 0x40e00000, v35
	v_min_f32_e32 v34, 0x40e00000, v34
	v_pk_mul_f32 v[40:41], v[34:35], s[34:35] op_sel_hi:[1,0]
	s_nop 0
	v_exp_f32_e32 v40, v40
	v_exp_f32_e32 v41, v41
	s_nop 0
	v_pk_add_f32 v[40:41], v[40:41], 1.0 op_sel_hi:[1,0]
	s_nop 0
	v_rcp_f32_e32 v40, v40
	v_rcp_f32_e32 v41, v41
	s_nop 0
	v_pk_mul_f32 v[34:35], v[34:35], v[40:41]
	s_nop 0
	v_pk_mul_f32 v[40:41], v[36:37], v[34:35]
	v_cvt_pk_bf16_f32 v34, v42, v43
	v_cvt_pk_bf16_f32 v35, v44, v45
	v_cvt_pk_bf16_f32 v36, v38, v39
	v_lshl_add_u64 v[38:39], s[14:15], 0, v[152:153]
	v_cvt_pk_bf16_f32 v37, v40, v41
	global_store_dwordx4 v[38:39], v[34:37], off
	s_add_i32 s14, s60, 0xa0
	s_ashr_i32 s15, s14, 31
	v_pk_mul_f32 v[34:35], v[30:31], s[34:35] op_sel_hi:[1,0]
	s_lshl_b64 s[14:15], s[14:15], 11
	v_exp_f32_e32 v34, v34
	v_exp_f32_e32 v35, v35
	s_add_u32 s1, s78, s14
	s_addc_u32 s2, s79, s15
	s_add_u32 s14, s1, s40
	v_pk_add_f32 v[34:35], v[34:35], 1.0 op_sel_hi:[1,0]
	s_addc_u32 s15, s2, s41
	v_rcp_f32_e32 v34, v34
	v_rcp_f32_e32 v35, v35
	s_nop 0
	v_pk_mul_f32 v[30:31], v[30:31], v[34:35]
	s_nop 0
	v_pk_mul_f32 v[26:27], v[26:27], v[30:31]
	v_pk_add_f32 v[30:31], v[32:33], v[74:75]
	s_nop 0
	v_min_f32_e32 v31, 0x40e00000, v31
	v_min_f32_e32 v30, 0x40e00000, v30
	v_pk_mul_f32 v[32:33], v[30:31], s[34:35] op_sel_hi:[1,0]
	s_nop 0
	v_exp_f32_e32 v32, v32
	v_exp_f32_e32 v33, v33
	s_nop 0
	v_pk_add_f32 v[32:33], v[32:33], 1.0 op_sel_hi:[1,0]
	s_nop 0
	v_rcp_f32_e32 v32, v32
	v_rcp_f32_e32 v33, v33
	s_nop 0
	v_pk_mul_f32 v[30:31], v[30:31], v[32:33]
	s_nop 0
	v_pk_mul_f32 v[28:29], v[28:29], v[30:31]
	v_pk_mul_f32 v[30:31], v[22:23], s[34:35] op_sel_hi:[1,0]
	s_nop 0
	v_exp_f32_e32 v30, v30
	v_exp_f32_e32 v31, v31
	s_nop 0
	v_pk_add_f32 v[30:31], v[30:31], 1.0 op_sel_hi:[1,0]
	s_nop 0
	v_rcp_f32_e32 v30, v30
	v_rcp_f32_e32 v31, v31
	s_nop 0
	v_pk_mul_f32 v[22:23], v[22:23], v[30:31]
	s_nop 0
	v_pk_mul_f32 v[22:23], v[18:19], v[22:23]
	v_pk_add_f32 v[18:19], v[24:25], v[58:59]
	s_nop 0
	v_min_f32_e32 v19, 0x40e00000, v19
	v_min_f32_e32 v18, 0x40e00000, v18
	v_pk_mul_f32 v[24:25], v[18:19], s[34:35] op_sel_hi:[1,0]
	s_nop 0
	v_exp_f32_e32 v24, v24
	v_exp_f32_e32 v25, v25
	s_nop 0
	v_pk_add_f32 v[24:25], v[24:25], 1.0 op_sel_hi:[1,0]
	s_nop 0
	v_rcp_f32_e32 v24, v24
	v_rcp_f32_e32 v25, v25
	s_nop 0
	v_pk_mul_f32 v[18:19], v[18:19], v[24:25]
	s_nop 0
	v_pk_mul_f32 v[24:25], v[20:21], v[18:19]
	v_cvt_pk_bf16_f32 v18, v26, v27
	v_cvt_pk_bf16_f32 v19, v28, v29
	v_cvt_pk_bf16_f32 v20, v22, v23
	v_lshl_add_u64 v[22:23], s[14:15], 0, v[152:153]
	v_cvt_pk_bf16_f32 v21, v24, v25
	global_store_dwordx4 v[22:23], v[18:21], off
	s_add_i32 s14, s60, 0xb0
	s_ashr_i32 s15, s14, 31
	v_pk_mul_f32 v[18:19], v[14:15], s[34:35] op_sel_hi:[1,0]
	s_lshl_b64 s[14:15], s[14:15], 11
	v_exp_f32_e32 v18, v18
	v_exp_f32_e32 v19, v19
	s_add_u32 s1, s78, s14
	s_addc_u32 s2, s79, s15
	s_add_u32 s14, s1, s40
	v_pk_add_f32 v[18:19], v[18:19], 1.0 op_sel_hi:[1,0]
	s_addc_u32 s15, s2, s41
	v_rcp_f32_e32 v18, v18
	v_rcp_f32_e32 v19, v19
	s_and_b64 vcc, exec, s[38:39]
	v_pk_mul_f32 v[14:15], v[14:15], v[18:19]
	s_nop 0
	v_pk_mul_f32 v[10:11], v[10:11], v[14:15]
	v_pk_add_f32 v[14:15], v[16:17], v[74:75]
	s_nop 0
	v_min_f32_e32 v15, 0x40e00000, v15
	v_min_f32_e32 v14, 0x40e00000, v14
	v_pk_mul_f32 v[16:17], v[14:15], s[34:35] op_sel_hi:[1,0]
	s_nop 0
	v_exp_f32_e32 v16, v16
	v_exp_f32_e32 v17, v17
	s_nop 0
	v_pk_add_f32 v[16:17], v[16:17], 1.0 op_sel_hi:[1,0]
	s_nop 0
	v_rcp_f32_e32 v16, v16
	v_rcp_f32_e32 v17, v17
	s_nop 0
	v_pk_mul_f32 v[14:15], v[14:15], v[16:17]
	s_nop 0
	v_pk_mul_f32 v[12:13], v[12:13], v[14:15]
	v_pk_mul_f32 v[14:15], v[6:7], s[34:35] op_sel_hi:[1,0]
	s_nop 0
	v_exp_f32_e32 v14, v14
	v_exp_f32_e32 v15, v15
	s_nop 0
	v_pk_add_f32 v[14:15], v[14:15], 1.0 op_sel_hi:[1,0]
	s_nop 0
	v_rcp_f32_e32 v14, v14
	v_rcp_f32_e32 v15, v15
	s_nop 0
	v_pk_mul_f32 v[6:7], v[6:7], v[14:15]
	s_nop 0
	v_pk_mul_f32 v[6:7], v[2:3], v[6:7]
	v_pk_add_f32 v[2:3], v[8:9], v[58:59]
	s_nop 0
	v_min_f32_e32 v3, 0x40e00000, v3
	v_min_f32_e32 v2, 0x40e00000, v2
	v_pk_mul_f32 v[8:9], v[2:3], s[34:35] op_sel_hi:[1,0]
	s_nop 0
	v_exp_f32_e32 v8, v8
	v_exp_f32_e32 v9, v9
	s_nop 0
	v_pk_add_f32 v[8:9], v[8:9], 1.0 op_sel_hi:[1,0]
	s_nop 0
	v_rcp_f32_e32 v8, v8
	v_rcp_f32_e32 v9, v9
	s_nop 0
	v_pk_mul_f32 v[2:3], v[2:3], v[8:9]
	s_nop 0
	v_pk_mul_f32 v[8:9], v[4:5], v[2:3]
	v_cvt_pk_bf16_f32 v2, v10, v11
	v_cvt_pk_bf16_f32 v3, v12, v13
	v_cvt_pk_bf16_f32 v4, v6, v7
	v_lshl_add_u64 v[6:7], s[14:15], 0, v[152:153]
	s_mov_b64 s[14:15], -1
	v_cvt_pk_bf16_f32 v5, v8, v9
	global_store_dwordx4 v[6:7], v[2:5], off
	s_cbranch_vccnz .LBB0_1325
	s_andn2_b64 vcc, exec, s[48:49]
	s_cbranch_vccnz .LBB0_1324
	s_branch .LBB0_1324

.LBB0_1462:
	s_cmp_lt_u32 s90, 2
	s_cbranch_scc1 .Ldn_norestore
	s_andn2_b64 vcc, exec, s[44:45]
	s_cbranch_vccnz .Ldn_norestore
	s_barrier

.LBB0_1466:
	s_lshl_b32 s15, s54, 8
	s_add_i32 s54, s15, s72
	s_ashr_i32 s55, s54, 31
	s_lshl_b64 s[24:25], s[54:55], 10
	s_add_u32 s24, s73, s24
	s_addc_u32 s25, s74, s25
	s_lshl_b32 s2, s42, 8
	s_ashr_i32 s14, s2, 31
	s_add_u32 s24, s24, s2
	s_addc_u32 s25, s25, s14
	s_add_u32 s24, s24, s29
	s_waitcnt vmcnt(0)
	v_pk_add_f32 v[138:139], v[10:11], v[138:139]
	v_mov_b32_e32 v157, v187
	s_addc_u32 s25, s25, 0
	v_cvt_pk_fp8_f32 v157, v138, v139
	v_lshl_add_u64 v[138:139], s[24:25], 0, v[150:151]
	s_add_i32 s24, s77, s15
	s_ashr_i32 s25, s24, 31
	s_lshl_b64 s[24:25], s[24:25], 10
	s_add_u32 s24, s73, s24
	s_addc_u32 s25, s74, s25
	s_add_u32 s24, s24, s2
	v_pk_add_f32 v[140:141], v[12:13], v[140:141]
	s_addc_u32 s25, s25, s14
	v_cvt_pk_fp8_f32 v157, v140, v141 op_sel:[0,0,1]
	v_pk_add_f32 v[130:131], v[2:3], v[130:131]
	v_mov_b32_e32 v141, v187
	s_add_u32 s24, s24, s29
	v_cvt_pk_fp8_f32 v141, v130, v131
	v_pk_add_f32 v[122:123], v[10:11], v[122:123]
	v_mov_b32_e32 v131, v187
	s_addc_u32 s25, s25, 0
	v_cvt_pk_fp8_f32 v131, v122, v123
	v_lshl_add_u64 v[122:123], s[24:25], 0, v[150:151]
	s_add_i32 s24, s78, s15
	s_ashr_i32 s25, s24, 31
	s_lshl_b64 s[24:25], s[24:25], 10
	s_add_u32 s24, s73, s24
	s_addc_u32 s25, s74, s25
	s_add_u32 s24, s24, s2
	v_pk_add_f32 v[124:125], v[12:13], v[124:125]
	s_addc_u32 s25, s25, s14
	v_cvt_pk_fp8_f32 v131, v124, v125 op_sel:[0,0,1]
	v_pk_add_f32 v[114:115], v[2:3], v[114:115]
	v_mov_b32_e32 v125, v187
	s_add_u32 s24, s24, s29
	v_cvt_pk_fp8_f32 v125, v114, v115
	v_pk_add_f32 v[106:107], v[10:11], v[106:107]
	v_mov_b32_e32 v115, v187
	s_addc_u32 s25, s25, 0
	v_cvt_pk_fp8_f32 v115, v106, v107
	v_lshl_add_u64 v[106:107], s[24:25], 0, v[150:151]
	s_add_i32 s24, s79, s15
	s_ashr_i32 s25, s24, 31
	s_lshl_b64 s[24:25], s[24:25], 10
	s_add_u32 s15, s73, s24
	s_addc_u32 s24, s74, s25
	s_add_u32 s15, s15, s2
	v_pk_add_f32 v[108:109], v[12:13], v[108:109]
	s_addc_u32 s25, s24, s14
	v_cvt_pk_fp8_f32 v115, v108, v109 op_sel:[0,0,1]
	v_pk_add_f32 v[98:99], v[2:3], v[98:99]
	v_mov_b32_e32 v109, v187
	s_add_u32 s24, s15, s29
	v_cvt_pk_fp8_f32 v109, v98, v99
	v_pk_add_f32 v[90:91], v[10:11], v[90:91]
	v_mov_b32_e32 v99, v187
	s_addc_u32 s25, s25, 0
	v_cvt_pk_fp8_f32 v99, v90, v91
	v_lshl_add_u64 v[90:91], s[24:25], 0, v[150:151]
	s_add_i32 s24, s54, 0x80
	s_ashr_i32 s25, s24, 31
	s_lshl_b64 s[24:25], s[24:25], 10
	s_add_u32 s15, s73, s24
	s_addc_u32 s24, s74, s25
	s_add_u32 s15, s15, s2
	v_pk_add_f32 v[92:93], v[12:13], v[92:93]
	s_addc_u32 s25, s24, s14
	v_cvt_pk_fp8_f32 v99, v92, v93 op_sel:[0,0,1]
	v_pk_add_f32 v[82:83], v[2:3], v[82:83]
	v_mov_b32_e32 v93, v187
	s_add_u32 s24, s15, s29
	v_cvt_pk_fp8_f32 v93, v82, v83
	v_pk_add_f32 v[74:75], v[10:11], v[74:75]
	v_mov_b32_e32 v83, v187
	s_addc_u32 s25, s25, 0
	v_cvt_pk_fp8_f32 v83, v74, v75
	v_lshl_add_u64 v[74:75], s[24:25], 0, v[150:151]
	s_add_i32 s24, s54, 0x90
	s_ashr_i32 s25, s24, 31
	s_lshl_b64 s[24:25], s[24:25], 10
	s_add_u32 s15, s73, s24
	s_addc_u32 s24, s74, s25
	s_add_u32 s15, s15, s2
	v_pk_add_f32 v[76:77], v[12:13], v[76:77]
	s_addc_u32 s25, s24, s14
	v_cvt_pk_fp8_f32 v83, v76, v77 op_sel:[0,0,1]
	v_pk_add_f32 v[66:67], v[2:3], v[66:67]
	v_mov_b32_e32 v77, v187
	s_add_u32 s24, s15, s29
	v_cvt_pk_fp8_f32 v77, v66, v67
	v_pk_add_f32 v[58:59], v[10:11], v[58:59]
	v_mov_b32_e32 v67, v187
	s_addc_u32 s25, s25, 0
	v_cvt_pk_fp8_f32 v67, v58, v59
	v_lshl_add_u64 v[58:59], s[24:25], 0, v[150:151]
	s_add_i32 s24, s54, 0xa0
	s_ashr_i32 s25, s24, 31
	s_lshl_b64 s[24:25], s[24:25], 10
	v_pk_add_f32 v[60:61], v[12:13], v[60:61]
	s_add_u32 s15, s73, s24
	v_cvt_pk_fp8_f32 v67, v60, v61 op_sel:[0,0,1]
	v_pk_add_f32 v[50:51], v[2:3], v[50:51]
	v_mov_b32_e32 v61, v187
	s_addc_u32 s24, s74, s25
	v_cvt_pk_fp8_f32 v61, v50, v51
	v_pk_add_f32 v[42:43], v[10:11], v[42:43]
	v_mov_b32_e32 v51, v187
	s_add_u32 s15, s15, s2
	v_pk_add_f32 v[10:11], v[10:11], v[26:27]
	v_mov_b32_e32 v27, v187
	v_cvt_pk_fp8_f32 v51, v42, v43
	s_addc_u32 s25, s24, s14
	v_cvt_pk_fp8_f32 v27, v10, v11
	s_add_u32 s24, s15, s29
	s_addc_u32 s25, s25, 0
	v_pk_add_f32 v[44:45], v[12:13], v[44:45]
	v_lshl_add_u64 v[42:43], s[24:25], 0, v[150:151]
	s_add_i32 s24, s54, 0xb0
	v_pk_add_f32 v[12:13], v[12:13], v[28:29]
	v_pk_add_f32 v[142:143], v[14:15], v[142:143]
	v_mov_b32_e32 v156, v187
	v_pk_add_f32 v[134:135], v[6:7], v[134:135]
	v_mov_b32_e32 v140, v187
	v_pk_add_f32 v[126:127], v[14:15], v[126:127]
	v_mov_b32_e32 v130, v187
	v_pk_add_f32 v[118:119], v[6:7], v[118:119]
	v_mov_b32_e32 v124, v187
	v_pk_add_f32 v[110:111], v[14:15], v[110:111]
	v_mov_b32_e32 v114, v187
	v_pk_add_f32 v[102:103], v[6:7], v[102:103]
	v_mov_b32_e32 v108, v187
	v_pk_add_f32 v[94:95], v[14:15], v[94:95]
	v_mov_b32_e32 v98, v187
	v_pk_add_f32 v[86:87], v[6:7], v[86:87]
	v_mov_b32_e32 v92, v187
	v_pk_add_f32 v[78:79], v[14:15], v[78:79]
	v_mov_b32_e32 v82, v187
	v_pk_add_f32 v[70:71], v[6:7], v[70:71]
	v_mov_b32_e32 v76, v187
	v_pk_add_f32 v[62:63], v[14:15], v[62:63]
	v_mov_b32_e32 v66, v187
	v_pk_add_f32 v[54:55], v[6:7], v[54:55]
	v_mov_b32_e32 v60, v187
	v_pk_add_f32 v[46:47], v[14:15], v[46:47]
	v_mov_b32_e32 v50, v187
	v_cvt_pk_fp8_f32 v51, v44, v45 op_sel:[0,0,1]
	v_pk_add_f32 v[38:39], v[6:7], v[38:39]
	v_pk_add_f32 v[34:35], v[2:3], v[34:35]
	v_mov_b32_e32 v44, v187
	v_mov_b32_e32 v45, v187
	s_ashr_i32 s25, s24, 31
	v_pk_add_f32 v[14:15], v[14:15], v[30:31]
	v_mov_b32_e32 v26, v187
	v_cvt_pk_fp8_f32 v27, v12, v13 op_sel:[0,0,1]
	v_pk_add_f32 v[6:7], v[6:7], v[22:23]
	v_pk_add_f32 v[2:3], v[2:3], v[18:19]
	v_mov_b32_e32 v12, v187
	v_mov_b32_e32 v13, v187
	v_cvt_pk_fp8_f32 v156, v142, v143
	v_cvt_pk_fp8_f32 v140, v134, v135
	v_cvt_pk_fp8_f32 v130, v126, v127
	v_cvt_pk_fp8_f32 v124, v118, v119
	v_cvt_pk_fp8_f32 v114, v110, v111
	v_cvt_pk_fp8_f32 v108, v102, v103
	v_cvt_pk_fp8_f32 v98, v94, v95
	v_cvt_pk_fp8_f32 v92, v86, v87
	v_cvt_pk_fp8_f32 v82, v78, v79
	v_cvt_pk_fp8_f32 v76, v70, v71
	v_cvt_pk_fp8_f32 v66, v62, v63
	v_cvt_pk_fp8_f32 v60, v54, v55
	v_cvt_pk_fp8_f32 v50, v46, v47
	v_cvt_pk_fp8_f32 v44, v38, v39
	v_cvt_pk_fp8_f32 v45, v34, v35
	s_lshl_b64 s[24:25], s[24:25], 10
	v_cvt_pk_fp8_f32 v26, v14, v15
	v_cvt_pk_fp8_f32 v12, v6, v7
	v_cvt_pk_fp8_f32 v13, v2, v3
	s_add_u32 s15, s73, s24
	s_addc_u32 s24, s74, s25
	v_pk_add_f32 v[144:145], v[16:17], v[144:145]
	v_pk_add_f32 v[136:137], v[8:9], v[136:137]
	v_pk_add_f32 v[132:133], v[4:5], v[132:133]
	v_pk_add_f32 v[128:129], v[16:17], v[128:129]
	v_pk_add_f32 v[120:121], v[8:9], v[120:121]
	v_pk_add_f32 v[116:117], v[4:5], v[116:117]
	v_pk_add_f32 v[112:113], v[16:17], v[112:113]
	v_pk_add_f32 v[104:105], v[8:9], v[104:105]
	v_pk_add_f32 v[100:101], v[4:5], v[100:101]
	v_pk_add_f32 v[96:97], v[16:17], v[96:97]
	v_pk_add_f32 v[88:89], v[8:9], v[88:89]
	v_pk_add_f32 v[84:85], v[4:5], v[84:85]
	v_pk_add_f32 v[80:81], v[16:17], v[80:81]
	v_pk_add_f32 v[72:73], v[8:9], v[72:73]
	v_pk_add_f32 v[68:69], v[4:5], v[68:69]
	v_pk_add_f32 v[64:65], v[16:17], v[64:65]
	v_pk_add_f32 v[56:57], v[8:9], v[56:57]
	v_pk_add_f32 v[52:53], v[4:5], v[52:53]
	v_pk_add_f32 v[48:49], v[16:17], v[48:49]
	v_pk_add_f32 v[40:41], v[8:9], v[40:41]
	v_pk_add_f32 v[36:37], v[4:5], v[36:37]
	v_pk_add_f32 v[16:17], v[16:17], v[32:33]
	s_add_u32 s2, s15, s2
	v_pk_add_f32 v[8:9], v[8:9], v[24:25]
	v_pk_add_f32 v[4:5], v[4:5], v[20:21]
	v_cvt_pk_fp8_f32 v156, v144, v145 op_sel:[0,0,1]
	v_cvt_pk_fp8_f32 v140, v136, v137 op_sel:[0,0,1]
	v_cvt_pk_fp8_f32 v141, v132, v133 op_sel:[0,0,1]
	v_cvt_pk_fp8_f32 v130, v128, v129 op_sel:[0,0,1]
	v_cvt_pk_fp8_f32 v124, v120, v121 op_sel:[0,0,1]
	v_cvt_pk_fp8_f32 v125, v116, v117 op_sel:[0,0,1]
	v_cvt_pk_fp8_f32 v114, v112, v113 op_sel:[0,0,1]
	v_cvt_pk_fp8_f32 v108, v104, v105 op_sel:[0,0,1]
	v_cvt_pk_fp8_f32 v109, v100, v101 op_sel:[0,0,1]
	v_cvt_pk_fp8_f32 v98, v96, v97 op_sel:[0,0,1]
	v_cvt_pk_fp8_f32 v92, v88, v89 op_sel:[0,0,1]
	v_cvt_pk_fp8_f32 v93, v84, v85 op_sel:[0,0,1]
	v_cvt_pk_fp8_f32 v82, v80, v81 op_sel:[0,0,1]
	v_cvt_pk_fp8_f32 v76, v72, v73 op_sel:[0,0,1]
	v_cvt_pk_fp8_f32 v77, v68, v69 op_sel:[0,0,1]
	v_cvt_pk_fp8_f32 v66, v64, v65 op_sel:[0,0,1]
	v_cvt_pk_fp8_f32 v60, v56, v57 op_sel:[0,0,1]
	v_cvt_pk_fp8_f32 v61, v52, v53 op_sel:[0,0,1]
	v_cvt_pk_fp8_f32 v50, v48, v49 op_sel:[0,0,1]
	v_cvt_pk_fp8_f32 v44, v40, v41 op_sel:[0,0,1]
	v_cvt_pk_fp8_f32 v45, v36, v37 op_sel:[0,0,1]
	v_cvt_pk_fp8_f32 v26, v16, v17 op_sel:[0,0,1]
	s_addc_u32 s15, s24, s14
	v_cvt_pk_fp8_f32 v12, v8, v9 op_sel:[0,0,1]
	v_cvt_pk_fp8_f32 v13, v4, v5 op_sel:[0,0,1]
	s_add_u32 s14, s2, s29
	s_addc_u32 s15, s15, 0
	v_lshl_add_u64 v[10:11], s[14:15], 0, v[150:151]
	s_mov_b64 s[14:15], -1
	s_andn2_b64 vcc, exec, s[38:39]
	global_store_dwordx2 v[138:139], v[156:157], off
	global_store_dwordx2 v[138:139], v[140:141], off offset:128
	global_store_dwordx2 v[122:123], v[130:131], off
	global_store_dwordx2 v[122:123], v[124:125], off offset:128
	global_store_dwordx2 v[106:107], v[114:115], off
	global_store_dwordx2 v[106:107], v[108:109], off offset:128
	global_store_dwordx2 v[90:91], v[98:99], off
	global_store_dwordx2 v[90:91], v[92:93], off offset:128
	global_store_dwordx2 v[74:75], v[82:83], off
	global_store_dwordx2 v[74:75], v[76:77], off offset:128
	global_store_dwordx2 v[58:59], v[66:67], off
	global_store_dwordx2 v[58:59], v[60:61], off offset:128
	global_store_dwordx2 v[42:43], v[50:51], off
	global_store_dwordx2 v[42:43], v[44:45], off offset:128
	global_store_dwordx2 v[10:11], v[26:27], off
	global_store_dwordx2 v[10:11], v[12:13], off offset:128
	s_cbranch_vccnz .LBB0_1453
	s_ashr_i32 s49, s48, 31
	s_lshl_b64 s[14:15], s[48:49], 12
	s_add_u32 s2, s16, s14
	s_addc_u32 s24, s17, s15
	s_lshl_b32 s14, s42, 8
	s_ashr_i32 s15, s14, 31
	s_lshl_b64 s[14:15], s[14:15], 2
	s_add_u32 s2, s2, s14
	s_addc_u32 s15, s24, s15
	s_add_u32 s14, s2, s43
	s_addc_u32 s15, s15, 0
	v_lshl_add_u64 v[6:7], s[14:15], 0, v[148:149]
	global_load_dwordx4 v[10:13], v[6:7], off offset:16
	global_load_dwordx4 v[14:17], v[6:7], off
	global_load_dwordx4 v[2:5], v[6:7], off offset:528
	s_nop 0
	global_load_dwordx4 v[6:9], v[6:7], off offset:512
	s_andn2_b64 vcc, exec, s[44:45]
	s_cbranch_vccnz .LBB0_1452
	s_branch .LBB0_1452
